# late_work drain loops: next tile claim (atomic) prefetched right after the current tile index is known, overlapping the claim round trip with the tile loads
# speedup vs baseline: 1.0032x; 1.0032x over previous
.LBB0_1006:
	v_mov_b32_e32 v1, v0
	s_barrier
	s_mov_b32 s9, 0
	v_cmp_eq_u32_e64 s[6:7], 0, v1
	v_mov_b32_e32 v11, 0
	s_mov_b32 s19, 0x8bff
	s_mov_b32 s20, 0x40000
	s_mov_b32 s21, 0x80000
	s_mov_b32 s22, 0xc0000
	s_movk_i32 s23, 0x204
	s_movk_i32 s24, 0x6000
	s_movk_i32 s25, 0xb00
	s_movk_i32 s26, 0x1600
	s_barrier
	s_mov_b32 s98, 0
	s_branch .LBB0_1009

.LBB0_1009:
	s_and_saveexec_b64 s[10:11], s[6:7]
	s_cbranch_execz .LBB0_1013
	s_cmp_lg_u32 s98, 0
	s_cbranch_scc1 .Lpfu_0
	s_mov_b64 s[14:15], exec
	v_mbcnt_lo_u32_b32 v1, s14, 0
	v_mbcnt_hi_u32_b32 v1, s15, v1
	v_cmp_eq_u32_e32 vcc, 0, v1
	s_and_saveexec_b64 s[12:13], vcc
	s_cbranch_execz .LBB0_1012
	s_bcnt1_i32_b64 s8, s[14:15]
	v_mov_b32_e32 v2, s8
	global_atomic_add v2, v11, v2, s[76:77] offset:512 sc0
.LBB0_1012:
	s_or_b64 exec, exec, s[12:13]
	s_waitcnt vmcnt(0)
	v_readfirstlane_b32 s8, v2
	s_nop 1
	v_add_u32_e32 v1, s8, v1
	ds_write_b32 v11, v1 offset:40960
	s_branch .LBB0_1013
.Lpfu_0:
	s_waitcnt vmcnt(2)
	ds_write_b32 v11, v249 offset:40960
.LBB0_1013:
	s_or_b64 exec, exec, s[10:11]
	s_waitcnt lgkmcnt(0)
	s_barrier
	ds_read_b32 v1, v11 offset:40960
	s_mov_b64 s[10:11], -1
	s_waitcnt lgkmcnt(0)
	v_cmp_lt_u32_e32 vcc, s19, v1
	v_readfirstlane_b32 s14, v1
	s_cbranch_vccnz .LBB0_1008
	s_mov_b32 s98, 0
	s_cmp_gt_u32 s14, 0x41ff
	s_cbranch_scc1 .Lpfs_0
	s_mov_b32 s98, 1
	s_and_saveexec_b64 s[100:101], s[6:7]
	s_cbranch_execz .Lpfn_0
	v_mov_b32_e32 v250, 1
	global_atomic_add v249, v11, v250, s[76:77] offset:512 sc0
.Lpfn_0:
	s_or_b64 exec, exec, s[100:101]
.Lpfs_0:
	s_cmpk_lt_u32 s14, 0x4a00
	s_cbranch_scc0 .LBB0_1022
	s_cmpk_gt_u32 s14, 0x41ff
	s_cbranch_scc0 .LBB0_1021
	s_cmpk_gt_u32 s14, 0x47ff
	s_cbranch_scc0 .LBB0_1018
	s_add_i32 s8, s14, 0xffffb800
	s_lshr_b32 s12, s8, 4
	s_lshl_b32 s10, s12, 11
	s_lshl_b32 s8, s8, 7
	s_sub_i32 s10, s8, s10
	s_ashr_i32 s11, s10, 31
	s_lshl_b32 s8, s12, 6
	s_lshl_b64 s[12:13], s[10:11], 13
	s_add_u32 s15, s72, s12
	v_mov_b32_e32 v1, v0
	s_addc_u32 s27, s73, s13
	s_lshl_b64 s[12:13], s[8:9], 2
	s_add_u32 s12, s15, s12
	v_lshlrev_b32_e32 v2, 2, v1
	v_ashrrev_i32_e32 v12, 4, v1
	v_and_b32_e32 v24, 60, v2
	s_addc_u32 s13, s27, s13
	v_lshlrev_b32_e32 v10, 2, v24
	v_ashrrev_i32_e32 v13, 31, v12
	v_lshl_add_u64 v[2:3], s[12:13], 0, v[10:11]
	v_lshlrev_b64 v[4:5], 13, v[12:13]
	v_lshl_add_u64 v[14:15], v[2:3], 0, v[4:5]
	v_add_co_u32_e32 v6, vcc, s20, v14
	v_ashrrev_i32_e32 v22, 3, v1
	s_nop 0
	v_addc_co_u32_e32 v7, vcc, 0, v15, vcc
	v_add_co_u32_e32 v16, vcc, s21, v14
	global_load_dwordx4 v[2:5], v[14:15], off
	s_nop 0
	global_load_dwordx4 v[6:9], v[6:7], off
	v_addc_co_u32_e32 v17, vcc, 0, v15, vcc
	v_add_co_u32_e32 v18, vcc, s22, v14
	v_lshlrev_b32_e32 v1, 4, v1
	s_nop 0
	v_addc_co_u32_e32 v19, vcc, 0, v15, vcc
	global_load_dwordx4 v[14:17], v[16:17], off
	s_nop 0
	global_load_dwordx4 v[18:21], v[18:19], off
	v_lshlrev_b32_e32 v10, 2, v12
	v_ashrrev_i32_e32 v23, 31, v22
	v_mul_u32_u24_e32 v24, 0x204, v24
	v_mul_lo_u32 v25, v22, s23
	v_lshlrev_b64 v[12:13], 12, v[22:23]
	v_add3_u32 v22, 0, v10, v24
	v_and_b32_e32 v10, 0x70, v1
	v_lshlrev_b32_e32 v1, 2, v10
	v_add3_u32 v1, 0, v25, v1
	v_add_u32_e32 v23, 0x400, v22
	s_lshl_b64 s[12:13], s[8:9], 12
	s_waitcnt vmcnt(63) expcnt(7) lgkmcnt(15)
	s_barrier
	s_add_u32 s8, s0, s12
	s_addc_u32 s12, s1, s13
	s_lshl_b64 s[10:11], s[10:11], 1
	s_add_u32 s10, s8, s10
	s_addc_u32 s11, s12, s11
	v_lshl_add_u64 v[12:13], s[10:11], 0, v[12:13]
	s_mov_b64 s[10:11], 0
	s_waitcnt vmcnt(2)
	ds_write2_b32 v22, v2, v6 offset1:32
	ds_write2_b32 v22, v3, v7 offset0:129 offset1:161
	ds_write2_b32 v23, v4, v8 offset0:2 offset1:34
	ds_write2_b32 v23, v5, v9 offset0:131 offset1:163
	s_waitcnt vmcnt(0)
	ds_write2_b32 v22, v14, v18 offset0:64 offset1:96
	ds_write2_b32 v22, v15, v19 offset0:193 offset1:225
	ds_write2_b32 v23, v16, v20 offset0:66 offset1:98
	ds_write2_b32 v23, v17, v21 offset0:195 offset1:227
	s_waitcnt lgkmcnt(0)
	s_barrier
	ds_read2_b32 v[2:3], v1 offset1:1
	ds_read2_b32 v[4:5], v1 offset0:2 offset1:3
	ds_read2_b32 v[6:7], v1 offset0:4 offset1:5
	ds_read2_b32 v[8:9], v1 offset0:6 offset1:7
	ds_read2_b32 v[14:15], v1 offset0:8 offset1:9
	ds_read2_b32 v[16:17], v1 offset0:10 offset1:11
	ds_read2_b32 v[18:19], v1 offset0:12 offset1:13
	ds_read2_b32 v[20:21], v1 offset0:14 offset1:15
	s_waitcnt lgkmcnt(7)
	v_cvt_pk_bf16_f32 v2, v2, v3
	s_waitcnt lgkmcnt(6)
	v_cvt_pk_bf16_f32 v3, v4, v5
	s_waitcnt lgkmcnt(5)
	v_cvt_pk_bf16_f32 v4, v6, v7
	s_waitcnt lgkmcnt(4)
	v_cvt_pk_bf16_f32 v5, v8, v9
	s_waitcnt lgkmcnt(3)
	v_cvt_pk_bf16_f32 v6, v14, v15
	s_waitcnt lgkmcnt(2)
	v_cvt_pk_bf16_f32 v7, v16, v17
	s_waitcnt lgkmcnt(1)
	v_cvt_pk_bf16_f32 v8, v18, v19
	s_waitcnt lgkmcnt(0)
	v_cvt_pk_bf16_f32 v9, v20, v21

.LBB0_1318:
	s_or_b64 exec, exec, s[22:23]
	s_add_u32 s0, s18, 0x3800000
	s_addc_u32 s1, s19, 0
	s_add_u32 s3, s18, 0x2000000
	s_addc_u32 s4, s19, 0
	s_add_u32 s5, s18, 0x1a000000
	s_addc_u32 s28, s19, 0
	v_mov_b32_e32 v1, v0
	s_add_u32 s29, s18, 0x4000000
	s_barrier
	s_mov_b32 s21, 0
	v_cmp_eq_u32_e64 s[6:7], 0, v1
	s_addc_u32 s30, s19, 0
	v_mov_b32_e32 v11, 0
	s_mov_b32 s31, 0x8bff
	s_mov_b32 s33, 0x40000
	s_mov_b32 s34, 0x80000
	s_mov_b32 s35, 0xc0000
	s_movk_i32 s36, 0x204
	s_movk_i32 s37, 0x6000
	s_movk_i32 s38, 0xb00
	s_movk_i32 s39, 0x1600
	s_barrier
	s_mov_b32 s98, 0
	s_branch .LBB0_1321

.LBB0_1321:
	s_and_saveexec_b64 s[22:23], s[6:7]
	s_cbranch_execz .LBB0_1325
	s_cmp_lg_u32 s98, 0
	s_cbranch_scc1 .Lpfu_1
	s_mov_b64 s[26:27], exec
	v_mbcnt_lo_u32_b32 v1, s26, 0
	v_mbcnt_hi_u32_b32 v1, s27, v1
	v_cmp_eq_u32_e32 vcc, 0, v1
	s_and_saveexec_b64 s[24:25], vcc
	s_cbranch_execz .LBB0_1324
	s_bcnt1_i32_b64 s20, s[26:27]
	v_mov_b32_e32 v2, s20
	global_atomic_add v2, v11, v2, s[18:19] offset:512 sc0
.LBB0_1324:
	s_or_b64 exec, exec, s[24:25]
	s_waitcnt vmcnt(0)
	v_readfirstlane_b32 s20, v2
	s_nop 1
	v_add_u32_e32 v1, s20, v1
	ds_write_b32 v11, v1 offset:40960
	s_branch .LBB0_1325

.LBB0_1325:
	s_or_b64 exec, exec, s[22:23]
	s_waitcnt lgkmcnt(0)
	s_barrier
	ds_read_b32 v1, v11 offset:40960
	s_mov_b64 s[22:23], -1
	s_waitcnt lgkmcnt(0)
	v_cmp_lt_u32_e32 vcc, s31, v1
	v_readfirstlane_b32 s26, v1
	s_cbranch_vccnz .LBB0_1320
	s_mov_b32 s98, 0
	s_cmp_gt_u32 s26, 0x49ff
	s_cbranch_scc1 .Lpfs_1
	s_mov_b32 s98, 1
	s_and_saveexec_b64 s[100:101], s[6:7]
	s_cbranch_execz .Lpfn_1
	v_mov_b32_e32 v250, 1
	global_atomic_add v249, v11, v250, s[18:19] offset:512 sc0

.Lpfs_1:
	s_cmpk_lt_u32 s26, 0x4a00
	s_cbranch_scc0 .LBB0_1334
	s_cmpk_gt_u32 s26, 0x41ff
	s_cbranch_scc0 .LBB0_1333
	s_cmpk_gt_u32 s26, 0x47ff
	s_cbranch_scc0 .LBB0_1330
	s_add_i32 s20, s26, 0xffffb800
	s_lshr_b32 s24, s20, 4
	s_lshl_b32 s22, s24, 11
	s_lshl_b32 s20, s20, 7
	s_sub_i32 s22, s20, s22
	s_ashr_i32 s23, s22, 31
	s_lshl_b32 s20, s24, 6
	s_lshl_b64 s[24:25], s[22:23], 13
	s_add_u32 s27, s14, s24
	v_mov_b32_e32 v1, v0
	s_addc_u32 s40, s15, s25
	s_lshl_b64 s[24:25], s[20:21], 2
	s_add_u32 s24, s27, s24
	v_lshlrev_b32_e32 v2, 2, v1
	v_ashrrev_i32_e32 v12, 4, v1
	v_and_b32_e32 v24, 60, v2
	s_addc_u32 s25, s40, s25
	v_lshlrev_b32_e32 v10, 2, v24
	v_ashrrev_i32_e32 v13, 31, v12
	v_lshl_add_u64 v[2:3], s[24:25], 0, v[10:11]
	v_lshlrev_b64 v[4:5], 13, v[12:13]
	v_lshl_add_u64 v[14:15], v[2:3], 0, v[4:5]
	v_add_co_u32_e32 v6, vcc, s33, v14
	v_ashrrev_i32_e32 v22, 3, v1
	s_nop 0
	v_addc_co_u32_e32 v7, vcc, 0, v15, vcc
	v_add_co_u32_e32 v16, vcc, s34, v14
	global_load_dwordx4 v[2:5], v[14:15], off
	s_nop 0
	global_load_dwordx4 v[6:9], v[6:7], off
	v_addc_co_u32_e32 v17, vcc, 0, v15, vcc
	v_add_co_u32_e32 v18, vcc, s35, v14
	v_lshlrev_b32_e32 v1, 4, v1
	s_nop 0
	v_addc_co_u32_e32 v19, vcc, 0, v15, vcc
	global_load_dwordx4 v[14:17], v[16:17], off
	s_nop 0
	global_load_dwordx4 v[18:21], v[18:19], off
	v_lshlrev_b32_e32 v10, 2, v12
	v_ashrrev_i32_e32 v23, 31, v22
	v_mul_u32_u24_e32 v24, 0x204, v24
	v_mul_lo_u32 v25, v22, s36
	v_lshlrev_b64 v[12:13], 12, v[22:23]
	v_add3_u32 v22, 0, v10, v24
	v_and_b32_e32 v10, 0x70, v1
	v_lshlrev_b32_e32 v1, 2, v10
	v_add3_u32 v1, 0, v25, v1
	v_add_u32_e32 v23, 0x400, v22
	s_lshl_b64 s[24:25], s[20:21], 12
	s_barrier
	s_add_u32 s20, s0, s24
	s_addc_u32 s24, s1, s25
	s_lshl_b64 s[22:23], s[22:23], 1
	s_add_u32 s22, s20, s22
	s_addc_u32 s23, s24, s23
	v_lshl_add_u64 v[12:13], s[22:23], 0, v[12:13]
	s_mov_b64 s[22:23], 0
	s_waitcnt vmcnt(2)
	ds_write2_b32 v22, v2, v6 offset1:32
	ds_write2_b32 v22, v3, v7 offset0:129 offset1:161
	ds_write2_b32 v23, v4, v8 offset0:2 offset1:34
	ds_write2_b32 v23, v5, v9 offset0:131 offset1:163
	s_waitcnt vmcnt(0)
	ds_write2_b32 v22, v14, v18 offset0:64 offset1:96
	ds_write2_b32 v22, v15, v19 offset0:193 offset1:225
	ds_write2_b32 v23, v16, v20 offset0:66 offset1:98
	ds_write2_b32 v23, v17, v21 offset0:195 offset1:227
	s_waitcnt lgkmcnt(0)
	s_barrier
	ds_read2_b32 v[2:3], v1 offset1:1
	ds_read2_b32 v[4:5], v1 offset0:2 offset1:3
	ds_read2_b32 v[6:7], v1 offset0:4 offset1:5
	ds_read2_b32 v[8:9], v1 offset0:6 offset1:7
	ds_read2_b32 v[14:15], v1 offset0:8 offset1:9
	ds_read2_b32 v[16:17], v1 offset0:10 offset1:11
	ds_read2_b32 v[18:19], v1 offset0:12 offset1:13
	ds_read2_b32 v[20:21], v1 offset0:14 offset1:15
	s_waitcnt lgkmcnt(7)
	v_cvt_pk_bf16_f32 v2, v2, v3
	s_waitcnt lgkmcnt(6)
	v_cvt_pk_bf16_f32 v3, v4, v5
	s_waitcnt lgkmcnt(5)
	v_cvt_pk_bf16_f32 v4, v6, v7
	s_waitcnt lgkmcnt(4)
	v_cvt_pk_bf16_f32 v5, v8, v9
	s_waitcnt lgkmcnt(3)
	v_cvt_pk_bf16_f32 v6, v14, v15
	s_waitcnt lgkmcnt(2)
	v_cvt_pk_bf16_f32 v7, v16, v17
	s_waitcnt lgkmcnt(1)
	v_cvt_pk_bf16_f32 v8, v18, v19
	s_waitcnt lgkmcnt(0)
	v_cvt_pk_bf16_f32 v9, v20, v21

.LBB0_2002:
	v_mov_b32_e32 v1, v0
	s_barrier
	s_mov_b32 s9, 0
	v_cmp_eq_u32_e64 s[6:7], 0, v1
	v_mov_b32_e32 v11, 0
	s_mov_b32 s16, 0x8bff
	s_mov_b32 s17, 0x40000
	s_mov_b32 s21, 0x80000
	s_mov_b32 s22, 0xc0000
	s_movk_i32 s23, 0x204
	s_movk_i32 s24, 0x6000
	s_movk_i32 s25, 0xb00
	s_movk_i32 s26, 0x1600
	s_barrier
	s_mov_b32 s98, 0
	s_branch .LBB0_2005

.LBB0_2009:
	s_or_b64 exec, exec, s[10:11]
	s_waitcnt lgkmcnt(0)
	s_barrier
	ds_read_b32 v1, v11 offset:40960
	s_mov_b64 s[10:11], -1
	s_waitcnt lgkmcnt(0)
	v_cmp_lt_u32_e32 vcc, s16, v1
	v_readfirstlane_b32 s14, v1
	s_cbranch_vccnz .LBB0_2004
	s_mov_b32 s98, 0
	s_cmp_gt_u32 s14, 0x75ff
	s_cbranch_scc1 .Lpfs_2
	s_mov_b32 s98, 1
	s_and_saveexec_b64 s[100:101], s[6:7]
	s_cbranch_execz .Lpfn_2
	v_mov_b32_e32 v250, 1
	global_atomic_add v249, v11, v250, s[76:77] offset:512 sc0

.Lpfs_2:
	s_cmpk_lt_u32 s14, 0x4a00
	s_cbranch_scc0 .LBB0_2018
	s_cmpk_gt_u32 s14, 0x41ff
	s_cbranch_scc0 .LBB0_2017
	s_cmpk_gt_u32 s14, 0x47ff
	s_cbranch_scc0 .LBB0_2014
	s_add_i32 s8, s14, 0xffffb800
	s_lshr_b32 s12, s8, 4
	s_lshl_b32 s10, s12, 11
	s_lshl_b32 s8, s8, 7
	s_sub_i32 s10, s8, s10
	s_ashr_i32 s11, s10, 31
	s_lshl_b32 s8, s12, 6
	s_lshl_b64 s[12:13], s[10:11], 13
	s_add_u32 s15, s72, s12
	v_mov_b32_e32 v1, v0
	s_addc_u32 s27, s73, s13
	s_lshl_b64 s[12:13], s[8:9], 2
	s_add_u32 s12, s15, s12
	v_lshlrev_b32_e32 v2, 2, v1
	v_ashrrev_i32_e32 v12, 4, v1
	v_and_b32_e32 v24, 60, v2
	s_addc_u32 s13, s27, s13
	v_lshlrev_b32_e32 v10, 2, v24
	v_ashrrev_i32_e32 v13, 31, v12
	v_lshl_add_u64 v[2:3], s[12:13], 0, v[10:11]
	v_lshlrev_b64 v[4:5], 13, v[12:13]
	v_lshl_add_u64 v[14:15], v[2:3], 0, v[4:5]
	v_add_co_u32_e32 v6, vcc, s17, v14
	v_ashrrev_i32_e32 v22, 3, v1
	s_nop 0
	v_addc_co_u32_e32 v7, vcc, 0, v15, vcc
	v_add_co_u32_e32 v16, vcc, s21, v14
	global_load_dwordx4 v[2:5], v[14:15], off
	s_nop 0
	global_load_dwordx4 v[6:9], v[6:7], off
	v_addc_co_u32_e32 v17, vcc, 0, v15, vcc
	v_add_co_u32_e32 v18, vcc, s22, v14
	v_lshlrev_b32_e32 v1, 4, v1
	s_nop 0
	v_addc_co_u32_e32 v19, vcc, 0, v15, vcc
	global_load_dwordx4 v[14:17], v[16:17], off
	s_nop 0
	global_load_dwordx4 v[18:21], v[18:19], off
	v_lshlrev_b32_e32 v10, 2, v12
	v_ashrrev_i32_e32 v23, 31, v22
	v_mul_u32_u24_e32 v24, 0x204, v24
	v_mul_lo_u32 v25, v22, s23
	v_lshlrev_b64 v[12:13], 12, v[22:23]
	v_add3_u32 v22, 0, v10, v24
	v_and_b32_e32 v10, 0x70, v1
	v_lshlrev_b32_e32 v1, 2, v10
	v_add3_u32 v1, 0, v25, v1
	v_add_u32_e32 v23, 0x400, v22
	s_lshl_b64 s[12:13], s[8:9], 12
	s_waitcnt vmcnt(63) expcnt(7) lgkmcnt(15)
	s_barrier
	s_add_u32 s8, s0, s12
	s_addc_u32 s12, s1, s13
	s_lshl_b64 s[10:11], s[10:11], 1
	s_add_u32 s10, s8, s10
	s_addc_u32 s11, s12, s11
	v_lshl_add_u64 v[12:13], s[10:11], 0, v[12:13]
	s_mov_b64 s[10:11], 0
	s_waitcnt vmcnt(2)
	ds_write2_b32 v22, v2, v6 offset1:32
	ds_write2_b32 v22, v3, v7 offset0:129 offset1:161
	ds_write2_b32 v23, v4, v8 offset0:2 offset1:34
	ds_write2_b32 v23, v5, v9 offset0:131 offset1:163
	s_waitcnt vmcnt(0)
	ds_write2_b32 v22, v14, v18 offset0:64 offset1:96
	ds_write2_b32 v22, v15, v19 offset0:193 offset1:225
	ds_write2_b32 v23, v16, v20 offset0:66 offset1:98
	ds_write2_b32 v23, v17, v21 offset0:195 offset1:227
	s_waitcnt lgkmcnt(0)
	s_barrier
	ds_read2_b32 v[2:3], v1 offset1:1
	ds_read2_b32 v[4:5], v1 offset0:2 offset1:3
	ds_read2_b32 v[6:7], v1 offset0:4 offset1:5
	ds_read2_b32 v[8:9], v1 offset0:6 offset1:7
	ds_read2_b32 v[14:15], v1 offset0:8 offset1:9
	ds_read2_b32 v[16:17], v1 offset0:10 offset1:11
	ds_read2_b32 v[18:19], v1 offset0:12 offset1:13
	ds_read2_b32 v[20:21], v1 offset0:14 offset1:15
	s_waitcnt lgkmcnt(7)
	v_cvt_pk_bf16_f32 v2, v2, v3
	s_waitcnt lgkmcnt(6)
	v_cvt_pk_bf16_f32 v3, v4, v5
	s_waitcnt lgkmcnt(5)
	v_cvt_pk_bf16_f32 v4, v6, v7
	s_waitcnt lgkmcnt(4)
	v_cvt_pk_bf16_f32 v5, v8, v9
	s_waitcnt lgkmcnt(3)
	v_cvt_pk_bf16_f32 v6, v14, v15
	s_waitcnt lgkmcnt(2)
	v_cvt_pk_bf16_f32 v7, v16, v17
	s_waitcnt lgkmcnt(1)
	v_cvt_pk_bf16_f32 v8, v18, v19
	s_waitcnt lgkmcnt(0)
	v_cvt_pk_bf16_f32 v9, v20, v21

.LBB0_2132:
	v_mov_b32_e32 v1, v0
	s_barrier
	s_mov_b32 s21, 0
	v_cmp_eq_u32_e64 s[6:7], 0, v1
	v_mov_b32_e32 v11, 0
	s_mov_b32 s28, 0x8bff
	s_mov_b32 s29, 0x40000
	s_mov_b32 s34, 0x80000
	s_mov_b32 s35, 0xc0000
	s_movk_i32 s36, 0x204
	s_movk_i32 s37, 0x6000
	s_movk_i32 s38, 0xb00
	s_movk_i32 s39, 0x1600
	s_barrier
	s_mov_b32 s98, 0
	s_branch .LBB0_2135

.LBB0_2139:
	s_or_b64 exec, exec, s[22:23]
	s_waitcnt lgkmcnt(0)
	s_barrier
	ds_read_b32 v1, v11 offset:40960
	s_mov_b64 s[22:23], -1
	s_waitcnt lgkmcnt(0)
	v_cmp_lt_u32_e32 vcc, s28, v1
	v_readfirstlane_b32 s26, v1
	s_cbranch_vccnz .LBB0_2134
	s_mov_b32 s98, 0
	s_mov_b32 s98, 1
	s_and_saveexec_b64 s[100:101], s[6:7]
	s_cbranch_execz .Lpfn_3
	v_mov_b32_e32 v250, 1
	global_atomic_add v249, v11, v250, s[18:19] offset:512 sc0

.Lpfs_3:
	s_cmpk_lt_u32 s26, 0x4a00
	s_cbranch_scc0 .LBB0_2148
	s_cmpk_gt_u32 s26, 0x41ff
	s_cbranch_scc0 .LBB0_2147
	s_cmpk_gt_u32 s26, 0x47ff
	s_cbranch_scc0 .LBB0_2144
	s_add_i32 s20, s26, 0xffffb800
	s_lshr_b32 s24, s20, 4
	s_lshl_b32 s22, s24, 11
	s_lshl_b32 s20, s20, 7
	s_sub_i32 s22, s20, s22
	s_ashr_i32 s23, s22, 31
	s_lshl_b32 s20, s24, 6
	s_lshl_b64 s[24:25], s[22:23], 13
	s_add_u32 s27, s14, s24
	v_mov_b32_e32 v1, v0
	s_addc_u32 s40, s15, s25
	s_lshl_b64 s[24:25], s[20:21], 2
	s_add_u32 s24, s27, s24
	v_lshlrev_b32_e32 v2, 2, v1
	v_ashrrev_i32_e32 v12, 4, v1
	v_and_b32_e32 v24, 60, v2
	s_addc_u32 s25, s40, s25
	v_lshlrev_b32_e32 v10, 2, v24
	v_ashrrev_i32_e32 v13, 31, v12
	v_lshl_add_u64 v[2:3], s[24:25], 0, v[10:11]
	v_lshlrev_b64 v[4:5], 13, v[12:13]
	v_lshl_add_u64 v[14:15], v[2:3], 0, v[4:5]
	v_add_co_u32_e32 v6, vcc, s29, v14
	v_ashrrev_i32_e32 v22, 3, v1
	s_nop 0
	v_addc_co_u32_e32 v7, vcc, 0, v15, vcc
	v_add_co_u32_e32 v16, vcc, s34, v14
	global_load_dwordx4 v[2:5], v[14:15], off
	s_nop 0
	global_load_dwordx4 v[6:9], v[6:7], off
	v_addc_co_u32_e32 v17, vcc, 0, v15, vcc
	v_add_co_u32_e32 v18, vcc, s35, v14
	v_lshlrev_b32_e32 v1, 4, v1
	s_nop 0
	v_addc_co_u32_e32 v19, vcc, 0, v15, vcc
	global_load_dwordx4 v[14:17], v[16:17], off
	s_nop 0
	global_load_dwordx4 v[18:21], v[18:19], off
	v_lshlrev_b32_e32 v10, 2, v12
	v_ashrrev_i32_e32 v23, 31, v22
	v_mul_u32_u24_e32 v24, 0x204, v24
	v_mul_lo_u32 v25, v22, s36
	v_lshlrev_b64 v[12:13], 12, v[22:23]
	v_add3_u32 v22, 0, v10, v24
	v_and_b32_e32 v10, 0x70, v1
	v_lshlrev_b32_e32 v1, 2, v10
	v_add3_u32 v1, 0, v25, v1
	v_add_u32_e32 v23, 0x400, v22
	s_lshl_b64 s[24:25], s[20:21], 12
	s_barrier
	s_add_u32 s20, s0, s24
	s_addc_u32 s24, s1, s25
	s_lshl_b64 s[22:23], s[22:23], 1
	s_add_u32 s22, s20, s22
	s_addc_u32 s23, s24, s23
	v_lshl_add_u64 v[12:13], s[22:23], 0, v[12:13]
	s_mov_b64 s[22:23], 0
	s_waitcnt vmcnt(2)
	ds_write2_b32 v22, v2, v6 offset1:32
	ds_write2_b32 v22, v3, v7 offset0:129 offset1:161
	ds_write2_b32 v23, v4, v8 offset0:2 offset1:34
	ds_write2_b32 v23, v5, v9 offset0:131 offset1:163
	s_waitcnt vmcnt(0)
	ds_write2_b32 v22, v14, v18 offset0:64 offset1:96
	ds_write2_b32 v22, v15, v19 offset0:193 offset1:225
	ds_write2_b32 v23, v16, v20 offset0:66 offset1:98
	ds_write2_b32 v23, v17, v21 offset0:195 offset1:227
	s_waitcnt lgkmcnt(0)
	s_barrier
	ds_read2_b32 v[2:3], v1 offset1:1
	ds_read2_b32 v[4:5], v1 offset0:2 offset1:3
	ds_read2_b32 v[6:7], v1 offset0:4 offset1:5
	ds_read2_b32 v[8:9], v1 offset0:6 offset1:7
	ds_read2_b32 v[14:15], v1 offset0:8 offset1:9
	ds_read2_b32 v[16:17], v1 offset0:10 offset1:11
	ds_read2_b32 v[18:19], v1 offset0:12 offset1:13
	ds_read2_b32 v[20:21], v1 offset0:14 offset1:15
	s_waitcnt lgkmcnt(7)
	v_cvt_pk_bf16_f32 v2, v2, v3
	s_waitcnt lgkmcnt(6)
	v_cvt_pk_bf16_f32 v3, v4, v5
	s_waitcnt lgkmcnt(5)
	v_cvt_pk_bf16_f32 v4, v6, v7
	s_waitcnt lgkmcnt(4)
	v_cvt_pk_bf16_f32 v5, v8, v9
	s_waitcnt lgkmcnt(3)
	v_cvt_pk_bf16_f32 v6, v14, v15
	s_waitcnt lgkmcnt(2)
	v_cvt_pk_bf16_f32 v7, v16, v17
	s_waitcnt lgkmcnt(1)
	v_cvt_pk_bf16_f32 v8, v18, v19
	s_waitcnt lgkmcnt(0)
	v_cvt_pk_bf16_f32 v9, v20, v21
